# barrier 8 split by role re-applied with single-lane wait polls on top of the barrier 9 split
# baseline (speedup 1.0000x reference)
.LBB0_1443:
	s_cmp_lt_i32 s89, 32
	s_cbranch_scc1 .Lgw_end_8a
	s_cmpk_gt_i32 s89, 0xdf
	s_cbranch_scc1 .Lgw_end_8a
	s_cmp_lg_u32 s92, 0
	s_cbranch_scc1 .Lgw_end_8a
	s_mov_b64 exec, 1
	v_mov_b32_e32 v68, 0x22160
	ds_read_b32 v69, v68
	v_mov_b32_e32 v70, s99
	v_lshrrev_b32_e32 v71, 16, v70
	v_mov_b32_e32 v72, s98
	v_min_u32_e32 v72, 8, v72
	v_mov_b32_e32 v73, 0
	s_waitcnt lgkmcnt(0)
	v_mul_lo_u32 v72, v72, v69

.Lgw_end_8a:
	s_mov_b64 exec, -1
	s_waitcnt vmcnt(0) lgkmcnt(0)
	s_barrier

.LBB0_1449:
	v_add_u32_e32 v14, s14, v222
	v_ashrrev_i32_e32 v15, 31, v14
	v_lshlrev_b64 v[14:15], 11, v[14:15]
	v_lshl_add_u64 v[60:61], v[6:7], 0, v[14:15]
	v_add_co_u32_e32 v62, vcc, 0x8000, v60
	global_load_dwordx4 v[14:17], v[60:61], off
	global_load_dwordx4 v[18:21], v[4:5], off
	v_addc_co_u32_e32 v63, vcc, 0, v61, vcc
	v_add_co_u32_e32 v64, vcc, 0x10000, v60
	global_load_dwordx4 v[22:25], v[62:63], off
	s_nop 0
	v_addc_co_u32_e32 v65, vcc, 0, v61, vcc
	v_add_co_u32_e32 v66, vcc, 0x18000, v60
	global_load_dwordx4 v[26:29], v[64:65], off
	s_nop 0
	v_addc_co_u32_e32 v67, vcc, 0, v61, vcc
	global_load_dwordx4 v[30:33], v[66:67], off
	global_load_dwordx4 v[36:39], v[60:61], off offset:64
	global_load_dwordx4 v[40:43], v[4:5], off offset:64
	global_load_dwordx4 v[44:47], v[62:63], off offset:64
	global_load_dwordx4 v[48:51], v[64:65], off offset:64
	global_load_dwordx4 v[52:55], v[66:67], off offset:64
	s_and_b64 vcc, exec, s[4:5]
	s_waitcnt vmcnt(0)
	v_mfma_f32_16x16x32_bf16 v[14:17], v[14:17], v[18:21], 0
	v_mfma_f32_16x16x32_bf16 v[22:25], v[22:25], v[18:21], 0
	v_mfma_f32_16x16x32_bf16 v[26:29], v[26:29], v[18:21], 0
	v_mfma_f32_16x16x32_bf16 v[18:21], v[30:33], v[18:21], 0
	global_load_dwordx4 v[30:33], v[60:61], off offset:128
	global_load_dwordx4 v[56:59], v[4:5], off offset:128
	v_mfma_f32_16x16x32_bf16 v[14:17], v[36:39], v[40:43], v[14:17]
	global_load_dwordx4 v[36:39], v[62:63], off offset:128
	v_mfma_f32_16x16x32_bf16 v[22:25], v[44:47], v[40:43], v[22:25]
	global_load_dwordx4 v[44:47], v[64:65], off offset:128
	v_mfma_f32_16x16x32_bf16 v[26:29], v[48:51], v[40:43], v[26:29]
	global_load_dwordx4 v[48:51], v[66:67], off offset:128
	v_mfma_f32_16x16x32_bf16 v[18:21], v[52:55], v[40:43], v[18:21]
	global_load_dwordx4 v[40:43], v[60:61], off offset:192
	global_load_dwordx4 v[52:55], v[4:5], off offset:192
	s_waitcnt vmcnt(0)
	v_mfma_f32_16x16x32_bf16 v[14:17], v[30:33], v[56:59], v[14:17]
	global_load_dwordx4 v[30:33], v[62:63], off offset:192
	v_mfma_f32_16x16x32_bf16 v[22:25], v[36:39], v[56:59], v[22:25]
	global_load_dwordx4 v[36:39], v[64:65], off offset:192
	v_mfma_f32_16x16x32_bf16 v[26:29], v[44:47], v[56:59], v[26:29]
	global_load_dwordx4 v[44:47], v[66:67], off offset:192
	s_waitcnt lgkmcnt(0)
	s_barrier
	v_mfma_f32_16x16x32_bf16 v[18:21], v[48:51], v[56:59], v[18:21]
	v_mfma_f32_16x16x32_bf16 v[14:17], v[40:43], v[52:55], v[14:17]
	s_waitcnt vmcnt(2)
	v_mfma_f32_16x16x32_bf16 v[22:25], v[30:33], v[52:55], v[22:25]
	s_waitcnt vmcnt(1)
	v_mfma_f32_16x16x32_bf16 v[26:29], v[36:39], v[52:55], v[26:29]
	s_waitcnt vmcnt(0)
	v_mfma_f32_16x16x32_bf16 v[18:21], v[44:47], v[52:55], v[18:21]
	s_nop 1
	ds_write_b128 v34, v[14:17]
	s_nop 0
	ds_write_b128 v34, v[22:25] offset:1024
	s_nop 0
	ds_write_b128 v34, v[26:29] offset:2048
	s_nop 0
	ds_write_b128 v34, v[18:21] offset:3072
	s_waitcnt lgkmcnt(0)
	s_barrier
	s_cbranch_vccnz .LBB0_1448
	ds_read_b128 v[14:17], v1
	ds_read_b128 v[18:21], v1 offset:4096
	ds_read_b128 v[22:25], v1 offset:8192
	ds_read_b128 v[36:39], v1 offset:1024
	ds_read_b128 v[40:43], v1 offset:5120
	s_cmp_lt_i32 s19, 16
	s_waitcnt lgkmcnt(3)
	v_pk_add_f32 v[14:15], v[14:15], v[18:19]
	v_pk_add_f32 v[20:21], v[16:17], v[20:21]
	s_waitcnt lgkmcnt(2)
	v_pk_add_f32 v[30:31], v[14:15], v[22:23]
	s_mov_b64 exec, 1
	v_mov_b32_e32 v68, 0x22160
	ds_read_b32 v69, v68
	v_mov_b32_e32 v70, s99
	v_lshrrev_b32_e32 v71, 16, v70
	v_mov_b32_e32 v72, s98
	v_min_u32_e32 v72, 8, v72
	v_mov_b32_e32 v73, 0
	s_waitcnt lgkmcnt(0)
	v_mul_lo_u32 v72, v72, v69

.Lgw_end_8b:
	s_mov_b64 exec, -1
	global_load_dword v14, v[8:9], off
	ds_read_b128 v[16:19], v1 offset:9216
	v_pk_add_f32 v[28:29], v[20:21], v[24:25]
	ds_read_b128 v[24:27], v1 offset:12288
	ds_read_b128 v[20:23], v1 offset:16384
	ds_read_b128 v[44:47], v1 offset:13312
	s_cselect_b64 s[10:11], -1, 0
	s_cmp_gt_i32 s19, 15
	s_waitcnt lgkmcnt(2)
	v_pk_add_f32 v[28:29], v[28:29], v[26:27]
	v_pk_add_f32 v[30:31], v[30:31], v[24:25]
	ds_read_b128 v[24:27], v1 offset:20480
	ds_read_b128 v[48:51], v1 offset:17408
	s_waitcnt lgkmcnt(3)
	v_pk_add_f32 v[28:29], v[28:29], v[22:23]
	v_pk_add_f32 v[30:31], v[30:31], v[20:21]
	ds_read_b128 v[20:23], v1 offset:24576
	ds_read_b128 v[52:55], v1 offset:21504
	s_waitcnt lgkmcnt(3)
	v_pk_add_f32 v[28:29], v[28:29], v[26:27]
	v_pk_add_f32 v[30:31], v[30:31], v[24:25]
	ds_read_b128 v[24:27], v1 offset:28672
	ds_read_b128 v[56:59], v1 offset:25600
	s_waitcnt lgkmcnt(3)
	v_pk_add_f32 v[28:29], v[28:29], v[22:23]
	v_pk_add_f32 v[32:33], v[30:31], v[20:21]
	ds_read_b128 v[20:23], v1 offset:29696
	s_waitcnt lgkmcnt(2)
	v_pk_add_f32 v[30:31], v[28:29], v[26:27]
	v_pk_add_f32 v[28:29], v[32:33], v[24:25]
	v_pk_add_f32 v[24:25], v[38:39], v[42:43]
	v_pk_add_f32 v[26:27], v[36:37], v[40:41]
	v_pk_add_f32 v[18:19], v[24:25], v[18:19]
	v_pk_add_f32 v[16:17], v[26:27], v[16:17]
	v_pk_add_f32 v[18:19], v[18:19], v[46:47]
	v_pk_add_f32 v[16:17], v[16:17], v[44:45]
	v_pk_add_f32 v[18:19], v[18:19], v[50:51]
	v_pk_add_f32 v[16:17], v[16:17], v[48:49]
	v_pk_add_f32 v[18:19], v[18:19], v[54:55]
	v_pk_add_f32 v[16:17], v[16:17], v[52:53]
	s_waitcnt lgkmcnt(1)
	v_pk_add_f32 v[18:19], v[18:19], v[58:59]
	v_pk_add_f32 v[24:25], v[16:17], v[56:57]
	s_waitcnt lgkmcnt(0)
	v_pk_add_f32 v[26:27], v[18:19], v[22:23]
	ds_read_b128 v[16:19], v1 offset:2048
	ds_read_b128 v[36:39], v1 offset:6144
	v_pk_add_f32 v[24:25], v[24:25], v[20:21]
	ds_read_b128 v[20:23], v1 offset:10240
	ds_read_b128 v[40:43], v1 offset:3072
	ds_read_b128 v[44:47], v1 offset:7168
	s_waitcnt lgkmcnt(3)
	v_pk_add_f32 v[32:33], v[18:19], v[38:39]
	v_pk_add_f32 v[48:49], v[16:17], v[36:37]
	ds_read_b128 v[16:19], v1 offset:14336
	ds_read_b128 v[36:39], v1 offset:11264
	s_waitcnt lgkmcnt(4)
	v_pk_add_f32 v[32:33], v[32:33], v[22:23]
	v_pk_add_f32 v[52:53], v[48:49], v[20:21]
	ds_read_b128 v[20:23], v1 offset:18432
	ds_read_b128 v[48:51], v1 offset:15360
	s_waitcnt lgkmcnt(3)
	v_pk_add_f32 v[32:33], v[32:33], v[18:19]
	v_pk_add_f32 v[56:57], v[52:53], v[16:17]
	ds_read_b128 v[16:19], v1 offset:22528
	ds_read_b128 v[52:55], v1 offset:19456
	s_waitcnt lgkmcnt(3)
	v_pk_add_f32 v[32:33], v[32:33], v[22:23]
	v_pk_add_f32 v[60:61], v[56:57], v[20:21]
	ds_read_b128 v[20:23], v1 offset:26624
	ds_read_b128 v[56:59], v1 offset:23552
	s_waitcnt lgkmcnt(3)
	v_pk_add_f32 v[32:33], v[32:33], v[18:19]
	v_pk_add_f32 v[64:65], v[60:61], v[16:17]
	ds_read_b128 v[16:19], v1 offset:30720
	ds_read_b128 v[60:63], v1 offset:27648
	s_waitcnt lgkmcnt(3)
	v_pk_add_f32 v[22:23], v[32:33], v[22:23]
	v_pk_add_f32 v[20:21], v[64:65], v[20:21]
	ds_read_b128 v[64:67], v1 offset:31744
	s_waitcnt lgkmcnt(2)
	v_pk_add_f32 v[22:23], v[22:23], v[18:19]
	v_pk_add_f32 v[20:21], v[20:21], v[16:17]
	v_pk_add_f32 v[16:17], v[42:43], v[46:47]
	v_pk_add_f32 v[18:19], v[40:41], v[44:45]
	v_pk_add_f32 v[16:17], v[16:17], v[38:39]
	v_pk_add_f32 v[18:19], v[18:19], v[36:37]
	v_pk_add_f32 v[16:17], v[16:17], v[50:51]
	v_pk_add_f32 v[18:19], v[18:19], v[48:49]
	v_pk_add_f32 v[16:17], v[16:17], v[54:55]
	v_pk_add_f32 v[18:19], v[18:19], v[52:53]
	v_pk_add_f32 v[16:17], v[16:17], v[58:59]
	v_pk_add_f32 v[18:19], v[18:19], v[56:57]
	s_waitcnt lgkmcnt(1)
	v_pk_add_f32 v[16:17], v[16:17], v[62:63]
	v_pk_add_f32 v[32:33], v[18:19], v[60:61]
	s_waitcnt lgkmcnt(0)
	v_pk_add_f32 v[18:19], v[16:17], v[66:67]
	v_pk_add_f32 v[16:17], v[32:33], v[64:65]
	s_cbranch_scc1 .LBB0_1452
	v_pk_mul_f32 v[32:33], v[30:31], v[30:31]
	v_pk_mul_f32 v[36:37], v[28:29], v[28:29]
	v_mul_f32_e32 v13, v16, v16
	v_pk_mov_b32 v[38:39], v[36:37], v[32:33] op_sel:[1,0]
	v_mov_b32_e32 v37, v33
	v_pk_add_f32 v[32:33], v[38:39], v[36:37]
	v_pk_mul_f32 v[36:37], v[26:27], v[26:27]
	v_pk_mul_f32 v[38:39], v[24:25], v[24:25]
	v_mul_f32_e32 v15, v17, v17
	v_pk_mov_b32 v[40:41], v[38:39], v[36:37] op_sel:[1,0]
	v_mov_b32_e32 v39, v37
	v_pk_add_f32 v[36:37], v[40:41], v[38:39]
	v_pk_add_f32 v[32:33], v[32:33], v[32:33] op_sel:[0,1] op_sel_hi:[1,0]
	v_pk_add_f32 v[36:37], v[36:37], v[36:37] op_sel:[0,1] op_sel_hi:[1,0]
	v_mov_b32_e32 v33, v13
	v_mov_b32_e32 v37, v15
	v_pk_add_f32 v[32:33], v[32:33], v[36:37]
	v_mul_f32_e32 v36, v21, v21
	v_mul_f32_e32 v38, v18, v18
	v_pk_fma_f32 v[36:37], v[20:21], v[20:21], v[36:37] op_sel_hi:[1,1,0]
	v_mul_f32_e32 v40, v19, v19
	v_mov_b32_e32 v37, v38
	v_mul_f32_e32 v38, v23, v23
	v_pk_fma_f32 v[38:39], v[22:23], v[22:23], v[38:39] op_sel_hi:[1,1,0]
	v_xor_b32_e32 v15, 16, v35
	v_mov_b32_e32 v39, v40
	v_pk_add_f32 v[36:37], v[36:37], v[38:39]
	s_nop 0
	v_pk_add_f32 v[32:33], v[32:33], v[36:37]
	s_nop 0
	v_add_f32_e32 v13, v32, v33
	v_and_b32_e32 v32, 64, v35
	v_add_u32_e32 v32, 64, v32
	v_cmp_lt_i32_e32 vcc, v15, v32
	s_nop 1
	v_cndmask_b32_e32 v15, v35, v15, vcc
	v_lshlrev_b32_e32 v15, 2, v15
	ds_bpermute_b32 v15, v15, v13
	s_waitcnt lgkmcnt(0)
	v_add_f32_e32 v13, v13, v15
	v_xor_b32_e32 v15, 32, v35
	v_cmp_lt_i32_e32 vcc, v15, v32
	s_nop 1
	v_cndmask_b32_e32 v15, v35, v15, vcc
	v_lshlrev_b32_e32 v15, 2, v15
	ds_bpermute_b32 v15, v15, v13
	s_waitcnt lgkmcnt(0)
	v_add_f32_e32 v13, v13, v15
	s_waitcnt vmcnt(0)
	v_mul_f32_e32 v15, v14, v14
	v_mul_f32_e32 v15, 0x3c800000, v15
	v_fmaak_f32 v13, v15, v13, 0x358637bd
	v_mul_f32_e32 v15, 0x4b800000, v13
	v_cmp_gt_f32_e32 vcc, s16, v13
	s_nop 1
	v_cndmask_b32_e32 v13, v13, v15, vcc
	v_rsq_f32_e32 v13, v13
	s_nop 0
	v_mul_f32_e32 v15, 0x45800000, v13
	v_cndmask_b32_e32 v13, v13, v15, vcc
	v_mul_f32_e32 v14, v14, v13
